# moe_sort row-copy loop and merge-epilogue sunk gate load de-serialised; OG/KVB tile-major layouts; gla_c LDS-shared state; NA V fragment-major; reductions via DPP
# speedup vs baseline: 1.0248x; 1.0112x over previous
.LBB0_1136:
	s_cmp_eq_u32 s43, 1
	s_cselect_b32 s2, 0x2600, s68
	s_cmp_eq_u32 s43, 0
	v_lshl_add_u32 v186, s47, 8, v223
	v_lshl_or_b32 v182, s46, 8, v225
	s_cselect_b32 s18, 0x1e00, s2
	s_cselect_b32 s19, 0x2600, s68
	v_mov_b64_e32 v[122:123], s[8:9]
	v_mad_i64_i32 v[124:125], s[2:3], v186, s59, v[122:123]
	s_lshl_b32 s76, s18, 1
	v_ashrrev_i32_e32 v183, 31, v182
	s_lshl_b32 s18, s19, 1
	s_mov_b32 s19, s77
	v_lshl_add_u64 v[126:127], v[124:125], 0, s[76:77]
	v_lshlrev_b64 v[184:185], 1, v[182:183]
	v_lshl_add_u64 v[124:125], v[124:125], 0, s[18:19]
	v_or_b32_e32 v188, 16, v186
	v_lshl_add_u64 v[194:195], v[124:125], 0, v[184:185]
	v_mad_i64_i32 v[124:125], s[2:3], v188, s59, v[122:123]
	v_or_b32_e32 v190, 32, v186
	v_lshl_add_u64 v[126:127], v[126:127], 0, v[184:185]
	v_lshl_add_u64 v[128:129], v[124:125], 0, s[76:77]
	v_lshl_add_u64 v[124:125], v[124:125], 0, s[18:19]
	v_mad_i64_i32 v[122:123], s[2:3], v190, s59, v[122:123]
	global_load_dwordx4 v[170:173], v[126:127], off
	global_load_dwordx4 v[162:165], v[194:195], off offset:256
	v_lshl_add_u64 v[128:129], v[128:129], 0, v[184:185]
	v_lshl_add_u64 v[124:125], v[124:125], 0, v[184:185]
	global_load_dwordx4 v[166:169], v[126:127], off offset:256
	global_load_dwordx4 v[158:161], v[128:129], off
	global_load_dwordx4 v[154:157], v[124:125], off
	global_load_dwordx4 v[150:153], v[128:129], off offset:256
	v_lshl_add_u64 v[126:127], v[122:123], 0, s[76:77]
	v_lshl_add_u64 v[122:123], v[122:123], 0, s[18:19]
	v_lshl_add_u64 v[126:127], v[126:127], 0, v[184:185]
	v_lshl_add_u64 v[122:123], v[122:123], 0, v[184:185]
	global_load_dwordx4 v[146:149], v[124:125], off offset:256
	global_load_dwordx4 v[138:141], v[126:127], off
	global_load_dwordx4 v[134:137], v[122:123], off
	s_nop 0
	global_load_dwordx4 v[126:129], v[126:127], off offset:256
	s_nop 0
	global_load_dwordx4 v[122:125], v[122:123], off offset:256
	global_load_dwordx4 v[204:207], v[194:195], off
	v_ashrrev_i32_e32 v187, 31, v186
	v_lshlrev_b64 v[174:175], 12, v[186:187]
	v_lshl_add_u64 v[174:175], s[10:11], 0, v[174:175]
	s_cmp_gt_i32 s43, 1
	v_lshl_add_u64 v[178:179], v[182:183], 1, v[174:175]
	s_cselect_b64 s[20:21], -1, 0
	s_mov_b64 s[2:3], -1
	s_and_b64 vcc, exec, s[20:21]
	s_waitcnt vmcnt(0)
	v_lshlrev_b32_e32 v96, 16, v170
	v_and_b32_e32 v170, 0xffff0000, v170
	v_lshlrev_b32_e32 v174, 16, v171
	v_and_b32_e32 v171, 0xffff0000, v171
	v_lshlrev_b32_e32 v175, 16, v172
	v_and_b32_e32 v172, 0xffff0000, v172
	v_lshlrev_b32_e32 v176, 16, v173
	v_and_b32_e32 v173, 0xffff0000, v173
	v_max_f32_e32 v96, v96, v96
	v_max_f32_e32 v170, v170, v170
	v_max_f32_e32 v174, v174, v174
	v_max_f32_e32 v171, v171, v171
	v_max_f32_e32 v175, v175, v175
	v_max_f32_e32 v172, v172, v172
	v_max_f32_e32 v176, v176, v176
	v_max_f32_e32 v173, v173, v173
	v_max_f32_e32 v196, 0x1e3ce508, v96
	v_max_f32_e32 v197, 0x1e3ce508, v170
	v_max_f32_e32 v198, 0x1e3ce508, v174
	v_max_f32_e32 v199, 0x1e3ce508, v171
	v_max_f32_e32 v180, 0x1e3ce508, v175
	v_max_f32_e32 v181, 0x1e3ce508, v172
	v_max_f32_e32 v192, 0x1e3ce508, v176
	v_max_f32_e32 v193, 0x1e3ce508, v173
	s_cbranch_vccz .LBB0_1138
	v_pk_mul_f32 v[170:171], v[142:143], v[196:197]
	v_pk_mul_f32 v[172:173], v[130:131], v[180:181]
	v_pk_mul_f32 v[174:175], v[144:145], v[198:199]
	v_pk_mul_f32 v[176:177], v[132:133], v[192:193]
	v_cvt_pk_bf16_f32 v170, v170, v171
	v_cvt_pk_bf16_f32 v171, v174, v175
	v_cvt_pk_bf16_f32 v172, v172, v173
	v_cvt_pk_bf16_f32 v173, v176, v177
	global_store_dwordx4 v[178:179], v[170:173], off
	s_mov_b64 s[2:3], 0
.LBB0_1138:
	v_mov_b32_e32 v174, 0
	s_andn2_b64 vcc, exec, s[2:3]
	v_mov_b32_e32 v175, 0
	v_mov_b32_e32 v176, 0
	v_mov_b32_e32 v177, 0
	v_mov_b32_e32 v170, 0
	v_mov_b32_e32 v171, 0
	v_mov_b32_e32 v172, 0
	v_mov_b32_e32 v173, 0
	s_cbranch_vccnz .LBB0_1140
	v_mov_b32_e32 v170, v204
	v_mov_b32_e32 v171, v205
	v_mov_b32_e32 v172, v206
	v_mov_b32_e32 v173, v207
	v_and_b32_e32 v96, 0xffff0000, v170
	v_lshlrev_b32_e32 v170, 16, v170
	v_max_f32_e32 v96, v96, v96
	v_lshlrev_b32_e32 v174, 16, v171
	v_max_f32_e32 v170, v170, v170
	v_max_f32_e32 v96, 0x1e3ce508, v96
	v_and_b32_e32 v175, 0xffff0000, v171
	v_max_f32_e32 v170, 0x1e3ce508, v170
	v_rcp_f32_e32 v171, v96
	v_max_f32_e32 v96, v174, v174
	v_rcp_f32_e32 v170, v170
	v_max_f32_e32 v96, 0x1e3ce508, v96
	v_lshlrev_b32_e32 v176, 16, v172
	v_and_b32_e32 v177, 0xffff0000, v172
	v_rcp_f32_e32 v172, v96
	v_max_f32_e32 v96, v175, v175
	v_max_f32_e32 v96, 0x1e3ce508, v96
	v_lshlrev_b32_e32 v187, 16, v173
	v_and_b32_e32 v189, 0xffff0000, v173
	v_rcp_f32_e32 v173, v96
	v_max_f32_e32 v96, v176, v176
	v_pk_mul_f32 v[170:171], v[196:197], v[170:171]
	v_max_f32_e32 v96, 0x1e3ce508, v96
	v_pk_mul_f32 v[170:171], v[142:143], v[170:171]
	v_rcp_f32_e32 v142, v96
	v_max_f32_e32 v96, v177, v177
	v_max_f32_e32 v96, 0x1e3ce508, v96
	v_rcp_f32_e32 v143, v96
	v_max_f32_e32 v96, v187, v187
	v_pk_mul_f32 v[172:173], v[198:199], v[172:173]
	v_max_f32_e32 v96, 0x1e3ce508, v96
	v_pk_mul_f32 v[172:173], v[144:145], v[172:173]
	v_rcp_f32_e32 v144, v96
	v_max_f32_e32 v96, v189, v189
	v_max_f32_e32 v96, 0x1e3ce508, v96
	v_rcp_f32_e32 v145, v96
	v_pk_mul_f32 v[142:143], v[180:181], v[142:143]
	v_pk_mul_f32 v[144:145], v[192:193], v[144:145]
	s_nop 0
	v_pk_mul_f32 v[176:177], v[132:133], v[144:145]
	v_pk_mul_f32 v[174:175], v[130:131], v[142:143]

.LBB0_1687:
	s_or_b64 exec, exec, s[4:5]
	s_ashr_i32 s6, s16, 6
	s_add_u32 s4, s44, 0x74f8000
	s_addc_u32 s5, s45, 0
	s_cmp_gt_i32 s6, 63
	v_lshlrev_b32_e32 v96, 4, v0
	s_waitcnt lgkmcnt(0)
	s_barrier
	s_cbranch_scc1 .LBB0_1690
	v_lshl_add_u64 v[0:1], s[44:45], 0, v[96:97]
	s_mov_b64 s[10:11], 0x50f8000
	v_lshl_add_u64 v[0:1], v[0:1], 0, s[10:11]
	s_lshl_b32 s10, s6, 2
	s_add_i32 s10, s10, 0
	s_lshl_b32 s7, s34, 5
	v_lshl_add_u64 v[2:3], s[4:5], 0, v[96:97]
	s_add_i32 s10, s10, 64
	s_mov_b32 s11, s6
	s_waitcnt vmcnt(0)
	v_mov_b32_e32 v18, s10
	ds_read_b32 v32, v18
	s_ashr_i32 s12, s11, 1
	s_add_i32 s12, s12, s7
	s_ashr_i32 s13, s12, 31
	s_lshl_b64 s[12:13], s[12:13], 11
	v_lshl_add_u64 v[24:25], v[0:1], 0, s[12:13]
	global_load_dwordx4 v[40:43], v[24:25], off
	global_load_dwordx4 v[44:47], v[24:25], off offset:1024
	s_add_i32 s11, s11, 8
	s_add_i32 s10, s10, 32
	v_mov_b32_e32 v18, s10
	ds_read_b32 v33, v18
	s_ashr_i32 s12, s11, 1
	s_add_i32 s12, s12, s7
	s_ashr_i32 s13, s12, 31
	s_lshl_b64 s[12:13], s[12:13], 11
	v_lshl_add_u64 v[24:25], v[0:1], 0, s[12:13]
	global_load_dwordx4 v[48:51], v[24:25], off
	global_load_dwordx4 v[52:55], v[24:25], off offset:1024
	s_add_i32 s11, s11, 8
	s_add_i32 s10, s10, 32
	v_mov_b32_e32 v18, s10
	ds_read_b32 v34, v18
	s_ashr_i32 s12, s11, 1
	s_add_i32 s12, s12, s7
	s_ashr_i32 s13, s12, 31
	s_lshl_b64 s[12:13], s[12:13], 11
	v_lshl_add_u64 v[24:25], v[0:1], 0, s[12:13]
	global_load_dwordx4 v[56:59], v[24:25], off
	global_load_dwordx4 v[60:63], v[24:25], off offset:1024
	s_add_i32 s11, s11, 8
	s_add_i32 s10, s10, 32
	v_mov_b32_e32 v18, s10
	ds_read_b32 v35, v18
	s_ashr_i32 s12, s11, 1
	s_add_i32 s12, s12, s7
	s_ashr_i32 s13, s12, 31
	s_lshl_b64 s[12:13], s[12:13], 11
	v_lshl_add_u64 v[24:25], v[0:1], 0, s[12:13]
	global_load_dwordx4 v[64:67], v[24:25], off
	global_load_dwordx4 v[68:71], v[24:25], off offset:1024
	s_add_i32 s11, s11, 8
	s_add_i32 s10, s10, 32
	v_mov_b32_e32 v18, s10
	ds_read_b32 v36, v18
	s_ashr_i32 s12, s11, 1
	s_add_i32 s12, s12, s7
	s_ashr_i32 s13, s12, 31
	s_lshl_b64 s[12:13], s[12:13], 11
	v_lshl_add_u64 v[24:25], v[0:1], 0, s[12:13]
	global_load_dwordx4 v[72:75], v[24:25], off
	global_load_dwordx4 v[76:79], v[24:25], off offset:1024
	s_add_i32 s11, s11, 8
	s_add_i32 s10, s10, 32
	v_mov_b32_e32 v18, s10
	ds_read_b32 v37, v18
	s_ashr_i32 s12, s11, 1
	s_add_i32 s12, s12, s7
	s_ashr_i32 s13, s12, 31
	s_lshl_b64 s[12:13], s[12:13], 11
	v_lshl_add_u64 v[24:25], v[0:1], 0, s[12:13]
	global_load_dwordx4 v[80:83], v[24:25], off
	global_load_dwordx4 v[84:87], v[24:25], off offset:1024
	s_add_i32 s11, s11, 8
	s_add_i32 s10, s10, 32
	v_mov_b32_e32 v18, s10
	ds_read_b32 v38, v18
	s_ashr_i32 s12, s11, 1
	s_add_i32 s12, s12, s7
	s_ashr_i32 s13, s12, 31
	s_lshl_b64 s[12:13], s[12:13], 11
	v_lshl_add_u64 v[24:25], v[0:1], 0, s[12:13]
	global_load_dwordx4 v[88:91], v[24:25], off
	global_load_dwordx4 v[92:95], v[24:25], off offset:1024
	s_add_i32 s11, s11, 8
	s_add_i32 s10, s10, 32
	v_mov_b32_e32 v18, s10
	ds_read_b32 v39, v18
	s_ashr_i32 s12, s11, 1
	s_add_i32 s12, s12, s7
	s_ashr_i32 s13, s12, 31
	s_lshl_b64 s[12:13], s[12:13], 11
	v_lshl_add_u64 v[24:25], v[0:1], 0, s[12:13]
	global_load_dwordx4 v[100:103], v[24:25], off
	global_load_dwordx4 v[104:107], v[24:25], off offset:1024
	s_add_i32 s11, s11, 8
	s_add_i32 s10, s10, 32
	s_waitcnt lgkmcnt(0)
	v_ashrrev_i32_e32 v19, 31, v32
	v_mov_b32_e32 v18, v32
	v_lshlrev_b64 v[22:23], 11, v[18:19]
	v_lshl_add_u64 v[22:23], v[2:3], 0, v[22:23]
	s_waitcnt vmcnt(15)
	global_store_dwordx4 v[22:23], v[40:43], off
	s_waitcnt vmcnt(15)
	global_store_dwordx4 v[22:23], v[44:47], off offset:1024
	v_ashrrev_i32_e32 v19, 31, v33
	v_mov_b32_e32 v18, v33
	v_lshlrev_b64 v[22:23], 11, v[18:19]
	v_lshl_add_u64 v[22:23], v[2:3], 0, v[22:23]
	s_waitcnt vmcnt(15)
	global_store_dwordx4 v[22:23], v[48:51], off
	s_waitcnt vmcnt(15)
	global_store_dwordx4 v[22:23], v[52:55], off offset:1024
	v_ashrrev_i32_e32 v19, 31, v34
	v_mov_b32_e32 v18, v34
	v_lshlrev_b64 v[22:23], 11, v[18:19]
	v_lshl_add_u64 v[22:23], v[2:3], 0, v[22:23]
	s_waitcnt vmcnt(15)
	global_store_dwordx4 v[22:23], v[56:59], off
	s_waitcnt vmcnt(15)
	global_store_dwordx4 v[22:23], v[60:63], off offset:1024
	v_ashrrev_i32_e32 v19, 31, v35
	v_mov_b32_e32 v18, v35
	v_lshlrev_b64 v[22:23], 11, v[18:19]
	v_lshl_add_u64 v[22:23], v[2:3], 0, v[22:23]
	s_waitcnt vmcnt(15)
	global_store_dwordx4 v[22:23], v[64:67], off
	s_waitcnt vmcnt(15)
	global_store_dwordx4 v[22:23], v[68:71], off offset:1024
	v_ashrrev_i32_e32 v19, 31, v36
	v_mov_b32_e32 v18, v36
	v_lshlrev_b64 v[22:23], 11, v[18:19]
	v_lshl_add_u64 v[22:23], v[2:3], 0, v[22:23]
	s_waitcnt vmcnt(15)
	global_store_dwordx4 v[22:23], v[72:75], off
	s_waitcnt vmcnt(15)
	global_store_dwordx4 v[22:23], v[76:79], off offset:1024
	v_ashrrev_i32_e32 v19, 31, v37
	v_mov_b32_e32 v18, v37
	v_lshlrev_b64 v[22:23], 11, v[18:19]
	v_lshl_add_u64 v[22:23], v[2:3], 0, v[22:23]
	s_waitcnt vmcnt(15)
	global_store_dwordx4 v[22:23], v[80:83], off
	s_waitcnt vmcnt(15)
	global_store_dwordx4 v[22:23], v[84:87], off offset:1024
	v_ashrrev_i32_e32 v19, 31, v38
	v_mov_b32_e32 v18, v38
	v_lshlrev_b64 v[22:23], 11, v[18:19]
	v_lshl_add_u64 v[22:23], v[2:3], 0, v[22:23]
	s_waitcnt vmcnt(15)
	global_store_dwordx4 v[22:23], v[88:91], off
	s_waitcnt vmcnt(15)
	global_store_dwordx4 v[22:23], v[92:95], off offset:1024
	v_ashrrev_i32_e32 v19, 31, v39
	v_mov_b32_e32 v18, v39
	v_lshlrev_b64 v[22:23], 11, v[18:19]
	v_lshl_add_u64 v[22:23], v[2:3], 0, v[22:23]
	s_waitcnt vmcnt(15)
	global_store_dwordx4 v[22:23], v[100:103], off
	s_waitcnt vmcnt(15)
	global_store_dwordx4 v[22:23], v[104:107], off offset:1024
